# row pass A layer 1: both rows' bf16 loads of a trip issued together instead of load-wait-load-wait
# baseline (speedup 1.0000x reference)
.LBB0_370:
	v_add_u32_e32 v68, s34, v87
	v_cmp_gt_i32_e32 vcc, s77, v68
	s_or_b64 s[24:25], s[24:25], exec
	s_and_saveexec_b64 s[26:27], vcc
	s_cbranch_execz .LBB0_369
	v_mul_hi_i32 v34, v68, s38
	v_lshrrev_b32_e32 v35, 31, v34
	v_ashrrev_i32_e32 v34, 10, v34
	v_lshlrev_b32_e32 v90, 1, v68
	v_add_u32_e32 v62, v34, v35
	v_mad_i32_i24 v34, v62, s39, v90
	s_movk_i32 s12, 0xfff
	v_cmp_gt_i32_e64 s[10:11], s56, v34
	v_cmp_lt_i32_e64 s[12:13], s12, v34
	s_mov_b64 s[14:15], -1
	s_and_b64 vcc, exec, s[90:91]
	v_ashrrev_i32_e32 v91, 31, v90
	s_cbranch_vccz .LBB0_373
	v_lshlrev_b64 v[36:37], 11, v[90:91]
	v_lshl_add_u64 v[36:37], v[82:83], 0, v[36:37]
	global_load_dwordx2 v[38:39], v[36:37], off
	global_load_dwordx2 v[60:61], v[36:37], off offset:512
	global_load_dwordx2 v[42:43], v[36:37], off offset:1024
	global_load_dwordx2 v[44:45], v[36:37], off offset:1536
	global_load_dwordx2 v[52:53], v[36:37], off offset:2048
	global_load_dwordx2 v[48:49], v[36:37], off offset:2560
	global_load_dwordx2 v[40:41], v[36:37], off offset:3072
	global_load_dwordx2 v[36:37], v[36:37], off offset:3584
	s_mov_b64 s[14:15], 0
	s_waitcnt vmcnt(7)
	v_lshlrev_b32_e32 v70, 16, v38
	v_and_b32_e32 v71, 0xffff0000, v38
	v_lshlrev_b32_e32 v72, 16, v39
	v_and_b32_e32 v73, 0xffff0000, v39
	s_waitcnt vmcnt(6)
	v_lshlrev_b32_e32 v58, 16, v60
	v_and_b32_e32 v59, 0xffff0000, v60
	v_lshlrev_b32_e32 v60, 16, v61
	v_and_b32_e32 v61, 0xffff0000, v61
	s_waitcnt vmcnt(5)
	v_lshlrev_b32_e32 v54, 16, v42
	v_and_b32_e32 v55, 0xffff0000, v42
	v_lshlrev_b32_e32 v56, 16, v43
	v_and_b32_e32 v57, 0xffff0000, v43
	s_waitcnt vmcnt(4)
	v_lshlrev_b32_e32 v42, 16, v44
	v_and_b32_e32 v43, 0xffff0000, v44
	v_lshlrev_b32_e32 v44, 16, v45
	v_and_b32_e32 v45, 0xffff0000, v45

.LBB0_379:
	v_or_b32_e32 v92, 1, v90
	v_mul_hi_i32 v34, v92, s38
	v_lshrrev_b32_e32 v35, 31, v34
	v_ashrrev_i32_e32 v34, 11, v34
	v_add_u32_e32 v64, v34, v35
	v_mad_i32_i24 v66, v64, s39, v92
	s_movk_i32 s14, 0xfff
	v_cmp_gt_i32_e64 s[12:13], s56, v66
	v_cmp_lt_i32_e64 s[14:15], s14, v66
	s_mov_b64 s[28:29], -1
	s_and_b64 vcc, exec, s[6:7]
	v_ashrrev_i32_e32 v93, 31, v92
	s_cbranch_vccnz .LBB0_383
	s_waitcnt vmcnt(3)
	v_lshlrev_b32_e32 v50, 16, v52
	v_and_b32_e32 v51, 0xffff0000, v52
	v_lshlrev_b32_e32 v52, 16, v53
	v_and_b32_e32 v53, 0xffff0000, v53
	s_waitcnt vmcnt(2)
	v_lshlrev_b32_e32 v46, 16, v48
	v_and_b32_e32 v47, 0xffff0000, v48
	v_lshlrev_b32_e32 v48, 16, v49
	v_and_b32_e32 v49, 0xffff0000, v49
	s_waitcnt vmcnt(1)
	v_lshlrev_b32_e32 v38, 16, v40
	v_and_b32_e32 v39, 0xffff0000, v40
	v_lshlrev_b32_e32 v40, 16, v41
	v_and_b32_e32 v41, 0xffff0000, v41
	s_waitcnt vmcnt(0)
	v_lshlrev_b32_e32 v34, 16, v36
	v_and_b32_e32 v35, 0xffff0000, v36
	v_lshlrev_b32_e32 v36, 16, v37
	v_and_b32_e32 v37, 0xffff0000, v37
	s_cbranch_execz .LBB0_384
